# speedup vs baseline: 1.0046x; 1.0046x over previous
_Z8gemm16_kILi128ELi128ELi1ELi3EEvPKDF16_S1_PvPKfi:
	s_load_dwordx8 s[4:11], s[0:1], 0x0
	v_readfirstlane_b32 s3, v0
	s_cmpk_lt_i32 s3, 0x100
	s_cbranch_scc0 .LBB3_2
	s_setprio 1
